# compiled k3 loop (counted vmcnt) + sc1 write-through stores (k0,k3) + L2 warm-up of codebook fragments
# baseline (speedup 1.0000x reference)
.LBB2_414:
	s_movk_i32 s0, 0xc00
	v_mov_b64_e32 v[26:27], s[42:43]
	v_mul_u32_u24_e32 v28, 0xc00, v154
	v_mad_i64_i32 v[26:27], s[0:1], v62, s0, v[26:27]
	v_or_b32_e32 v28, v28, v98
	v_mov_b32_e32 v99, 0
	v_lshl_add_u64 v[26:27], v[26:27], 0, v[98:99]
	v_or_b32_e32 v29, 0x10000, v28
	global_store_dwordx4 v[26:27], v[22:25], off sc1
	ds_write_b128 v29, v[22:25]
	v_sub_f32_e32 v10, v10, v22
	v_or_b32_e32 v22, v101, v154
	v_sub_f32_e32 v11, v11, v23
	v_add_u32_e32 v23, v22, v102
	v_lshl_or_b32 v23, v23, 4, v103
	ds_write_b32 v23, v10
	v_add_u32_e32 v10, v22, v104
	v_lshl_or_b32 v10, v10, 4, v105
	ds_write_b32 v10, v11
	v_or_b32_e32 v10, v106, v154
	v_add_u32_e32 v10, v10, v107
	v_sub_f32_e32 v12, v12, v24
	v_lshl_or_b32 v10, v10, 4, v108
	ds_write_b32 v10, v12
	v_or_b32_e32 v10, v109, v154
	v_add_u32_e32 v10, v10, v110
	v_sub_f32_e32 v13, v13, v25
	v_lshl_or_b32 v10, v10, 4, v111
	ds_write_b32 v10, v13
	v_add_u32_e32 v10, 0x10400, v28
	ds_write_b128 v10, v[18:21]
	v_sub_f32_e32 v10, v6, v18
	v_sub_f32_e32 v11, v7, v19
	v_pk_add_f32 v[6:7], v[8:9], v[20:21] neg_lo:[0,1] neg_hi:[0,1]
	v_or_b32_e32 v8, v112, v154
	v_add_u32_e32 v9, v8, v113
	v_add_u32_e32 v8, v8, v115
	v_lshl_or_b32 v9, v9, 4, v114
	v_lshl_or_b32 v8, v8, 4, v116
	ds_write_b32 v9, v10
	ds_write_b32 v8, v11
	v_or_b32_e32 v8, v117, v154
	v_add_u32_e32 v8, v8, v118
	v_lshl_or_b32 v8, v8, 4, v119
	ds_write_b32 v8, v6
	v_or_b32_e32 v6, v120, v154
	v_add_u32_e32 v6, v6, v121
	v_lshl_or_b32 v6, v6, 4, v122
	ds_write_b32 v6, v7
	v_add_u32_e32 v6, 0x10800, v28
	ds_write_b128 v6, v[14:17]
	v_or_b32_e32 v6, v123, v154
	v_add_u32_e32 v7, v6, v124
	v_pk_add_f32 v[2:3], v[2:3], v[14:15] neg_lo:[0,1] neg_hi:[0,1]
	v_lshl_or_b32 v7, v7, 4, v125
	ds_write_b32 v7, v2
	v_add_u32_e32 v2, v6, v126
	v_lshl_or_b32 v2, v2, 4, v127
	ds_write_b32 v2, v3
	v_or_b32_e32 v2, v133, v154
	v_add_u32_e32 v2, v2, v134
	v_pk_add_f32 v[4:5], v[4:5], v[16:17] neg_lo:[0,1] neg_hi:[0,1]
	v_lshl_or_b32 v2, v2, 4, v63
	ds_write_b32 v2, v4
	v_or_b32_e32 v2, v135, v154
	v_add_u32_e32 v2, v2, v132
	v_lshl_or_b32 v2, v2, 4, v136
	v_add_lshl_u32 v4, v100, v154, 4
	s_mov_b32 s5, 0
	s_mov_b32 s4, 1.0
	ds_write_b32 v2, v5
	v_mov_b64_e32 v[2:3], s[4:5]
	v_add_u32_e32 v4, 8, v4
	s_waitcnt vmcnt(1)
	v_lshlrev_b32_e32 v40, 9, v150
	ds_write2st64_b64 v4, v[2:3], v[2:3] offset1:64
	v_or_b32_e32 v2, v40, v128
	v_lshlrev_b32_e32 v98, 4, v2
	v_lshl_add_u64 v[100:101], s[40:41], 0, v[98:99]
	s_mov_b64 s[0:1], 0x787000
	v_lshl_add_u64 v[34:35], v[100:101], 0, s[0:1]
	s_mov_b32 s0, 0x788000
	v_add_co_u32_e32 v36, vcc, s0, v100
	global_store_dwordx4 v[26:27], v[18:21], off offset:1024 sc1
	global_store_dwordx4 v[26:27], v[14:17], off offset:2048 sc1
	s_waitcnt lgkmcnt(0)
	s_barrier
	v_addc_co_u32_e32 v37, vcc, 0, v101, vcc
	s_lshr_b32 s59, s33, 4
	s_and_b32 s59, s59, 31
	s_lshl_b32 s59, s59, 15
	s_add_u32 s59, s59, 0x787000
	s_add_u32 s68, s40, s59
	s_addc_u32 s69, s41, 0
	v_lshlrev_b32_e32 v207, 6, v0
	global_load_dword v207, v207, s[68:69]
	global_load_dwordx4 v[2:5], v[34:35], off offset:1024
	global_load_dwordx4 v[10:13], v[34:35], off offset:2048
	global_load_dwordx4 v[14:17], v[34:35], off offset:3072
	global_load_dwordx4 v[6:9], v[36:37], off offset:-4096
	global_load_dwordx4 v[18:21], v[36:37], off
	global_load_dwordx4 v[22:25], v[36:37], off offset:1024
	global_load_dwordx4 v[26:29], v[36:37], off offset:2048
	global_load_dwordx4 v[30:33], v[36:37], off offset:3072
	v_and_b32_e32 v35, 15, v0
	v_lshrrev_b32_e32 v37, 4, v128
	v_lshlrev_b32_e32 v102, 2, v35
	v_lshlrev_b32_e32 v41, 2, v37
	v_lshlrev_b32_e32 v34, 4, v35
	v_cmp_gt_u32_e64 s[0:1], 6, v35
	v_mov_b32_e32 v35, v99
	v_or3_b32 v36, v34, v41, v40
	v_lshl_add_u64 v[104:105], s[44:45], 0, v[34:35]
	v_or_b32_e32 v34, v40, v34
	s_movk_i32 s4, 0x1000
	v_or3_b32 v153, v34, v41, s4
	v_or_b32_e32 v34, 0x11800, v98
	v_lshl_add_u64 v[118:119], s[40:41], 0, v[34:35]
	v_or_b32_e32 v34, 0x11400, v98
	v_lshl_add_u64 v[120:121], s[40:41], 0, v[34:35]
	v_or_b32_e32 v34, 0x11000, v98
	ds_read2st64_b32 v[132:133], v36 offset1:1
	v_or_b32_e32 v36, s33, v41
	v_lshl_add_u64 v[122:123], s[40:41], 0, v[34:35]
	v_or_b32_e32 v34, 0x10c00, v98
	v_or_b32_e32 v38, 1, v36
	v_lshl_add_u64 v[124:125], s[40:41], 0, v[34:35]
	v_or_b32_e32 v34, 0x10800, v98
	v_mul_u32_u24_e32 v152, 0x3000, v37
	v_ashrrev_i32_e32 v37, 31, v36
	v_ashrrev_i32_e32 v39, 31, v38
	v_lshl_add_u64 v[126:127], s[40:41], 0, v[34:35]
	v_or_b32_e32 v34, 0x10400, v98
	v_mov_b32_e32 v103, v99
	v_lshlrev_b64 v[108:109], 17, v[36:37]
	v_lshlrev_b64 v[110:111], 17, v[38:39]
	v_or_b32_e32 v38, 2, v36
	v_or_b32_e32 v36, 3, v36
	v_lshl_add_u64 v[128:129], s[40:41], 0, v[34:35]
	v_mul_u32_u24_e32 v34, 24, v150
	v_lshl_add_u64 v[106:107], s[38:39], 0, v[102:103]
	v_ashrrev_i32_e32 v39, 31, v38
	v_ashrrev_i32_e32 v37, 31, v36
	v_lshlrev_b32_e32 v103, 2, v0
	v_or_b32_e32 v98, 0x11c00, v98
	v_or_b32_e32 v34, v152, v34
	v_lshlrev_b64 v[112:113], 17, v[38:39]
	v_lshlrev_b64 v[114:115], 17, v[36:37]
	v_and_b32_e32 v116, 0x700, v103
	v_mov_b32_e32 v117, v99
	v_lshl_add_u64 v[130:131], s[40:41], 0, v[98:99]
	v_add_u32_e32 v154, v34, v102
	s_mov_b64 s[6:7], 0
	s_mov_b64 s[8:9], 0x800
	v_mov_b32_e32 v155, 0x400
	v_mov_b32_e32 v159, 0
	v_mov_b32_e32 v158, 0
	v_mov_b32_e32 v157, 0
	v_mov_b32_e32 v156, 0
	s_waitcnt vmcnt(0)
	s_branch .LBB2_417

.LBB2_416:
	s_or_b64 exec, exec, s[10:11]
	v_add_f32_e32 v64, v160, v161
	v_rcp_f32_e32 v64, v64
	v_add_f32_e32 v65, v163, v164
	v_lshl_add_u64 v[96:97], v[40:41], 2, v[104:105]
	v_rcp_f32_e32 v72, v65
	v_add_f32_e32 v48, v48, v56
	v_lshl_add_u64 v[40:41], v[96:97], 0, v[108:109]
	v_pk_mul_f32 v[134:135], v[64:65], v[134:135] op_sel_hi:[0,1]
	v_pk_mul_f32 v[136:137], v[64:65], v[136:137] op_sel_hi:[0,1]
	v_rcp_f32_e32 v56, v48
	global_store_dwordx4 v[40:41], v[134:137], off sc1
	v_add_f32_e32 v48, v49, v57
	v_rcp_f32_e32 v88, v48
	v_pk_mul_f32 v[134:135], v[64:65], v[138:139] op_sel_hi:[0,1]
	v_pk_mul_f32 v[136:137], v[64:65], v[140:141] op_sel_hi:[0,1]
	global_store_dwordx4 v[40:41], v[134:137], off offset:256 sc1
	v_pk_mul_f32 v[38:39], v[56:57], v[38:39] op_sel_hi:[0,1]
	s_add_u32 s6, s6, 0x10000
	v_pk_mul_f32 v[134:135], v[64:65], v[142:143] op_sel_hi:[0,1]
	v_pk_mul_f32 v[136:137], v[64:65], v[144:145] op_sel_hi:[0,1]
	global_store_dwordx4 v[40:41], v[134:137], off offset:512 sc1
	s_addc_u32 s7, s7, 0
	s_add_i32 s5, s5, 1
	v_pk_mul_f32 v[134:135], v[64:65], v[146:147] op_sel_hi:[0,1]
	v_pk_mul_f32 v[136:137], v[64:65], v[148:149] op_sel_hi:[0,1]
	global_store_dwordx4 v[40:41], v[134:137], off offset:768 sc1
	v_pk_mul_f32 v[40:41], v[72:73], v[42:43] op_sel_hi:[0,1]
	v_pk_mul_f32 v[42:43], v[72:73], v[34:35] op_sel_hi:[0,1]
	v_lshl_add_u64 v[134:135], v[96:97], 0, v[110:111]
	global_store_dwordx4 v[134:135], v[40:43], off offset:768 sc1
	v_lshl_add_u64 v[34:35], v[96:97], 0, v[112:113]
	v_pk_mul_f32 v[80:81], v[72:73], v[90:91] op_sel_hi:[0,1]
	v_pk_mul_f32 v[40:41], v[56:57], v[46:47] op_sel_hi:[0,1]
	global_store_dwordx4 v[34:35], v[38:41], off sc1
	v_lshl_add_u64 v[42:43], v[96:97], 0, v[114:115]
	v_pk_mul_f32 v[82:83], v[72:73], v[82:83] op_sel_hi:[0,1]
	v_pk_mul_f32 v[38:39], v[56:57], v[54:55] op_sel_hi:[0,1]
	v_pk_mul_f32 v[40:41], v[56:57], v[62:63] op_sel_hi:[0,1]
	global_store_dwordx4 v[34:35], v[38:41], off offset:256 sc1
	v_pk_mul_f32 v[64:65], v[72:73], v[74:75] op_sel_hi:[0,1]
	v_pk_mul_f32 v[66:67], v[72:73], v[66:67] op_sel_hi:[0,1]
	v_pk_mul_f32 v[38:39], v[56:57], v[70:71] op_sel_hi:[0,1]
	v_pk_mul_f32 v[40:41], v[56:57], v[78:79] op_sel_hi:[0,1]
	global_store_dwordx4 v[34:35], v[38:41], off offset:512 sc1
	v_pk_mul_f32 v[48:49], v[72:73], v[58:59] op_sel_hi:[0,1]
	v_pk_mul_f32 v[50:51], v[72:73], v[50:51] op_sel_hi:[0,1]
	v_pk_mul_f32 v[38:39], v[56:57], v[86:87] op_sel_hi:[0,1]
	v_pk_mul_f32 v[40:41], v[56:57], v[94:95] op_sel_hi:[0,1]
	global_store_dwordx4 v[34:35], v[38:41], off offset:768 sc1
	v_pk_mul_f32 v[34:35], v[88:89], v[44:45] op_sel_hi:[0,1]
	v_pk_mul_f32 v[36:37], v[88:89], v[36:37] op_sel_hi:[0,1]
	v_pk_mul_f32 v[38:39], v[88:89], v[92:93] op_sel_hi:[0,1]
	v_pk_mul_f32 v[40:41], v[88:89], v[84:85] op_sel_hi:[0,1]
	global_store_dwordx4 v[42:43], v[38:41], off sc1
	v_lshl_add_u64 v[116:117], v[116:117], 0, s[8:9]
	v_add_u32_e32 v153, 0x1000, v153
	v_pk_mul_f32 v[38:39], v[88:89], v[76:77] op_sel_hi:[0,1]
	v_pk_mul_f32 v[40:41], v[88:89], v[68:69] op_sel_hi:[0,1]
	global_store_dwordx4 v[42:43], v[38:41], off offset:256 sc1
	s_cmp_eq_u32 s6, 0x100000
	v_add_u32_e32 v154, 0xc0, v154
	v_pk_mul_f32 v[38:39], v[88:89], v[60:61] op_sel_hi:[0,1]
	v_pk_mul_f32 v[40:41], v[88:89], v[52:53] op_sel_hi:[0,1]
	global_store_dwordx4 v[134:135], v[80:83], off sc1
	global_store_dwordx4 v[134:135], v[64:67], off offset:256 sc1
	global_store_dwordx4 v[134:135], v[48:51], off offset:512 sc1
	global_store_dwordx4 v[42:43], v[38:41], off offset:512 sc1
	global_store_dwordx4 v[42:43], v[34:37], off offset:768 sc1
	s_cbranch_scc1 .LBB2_422
